# expert GEMM1 phase prologues: first unit's four token-index loads issued together with one wait (on top of v76)
# baseline (speedup 1.0000x reference)
.LBB0_978:
	s_andn2_b64 vcc, exec, s[6:7]
	s_cbranch_vccnz .LBB0_1031
	s_add_u32 s4, s22, 0x18400000
	s_addc_u32 s5, s23, 0
	s_add_i32 s3, s33, 0
	s_add_i32 s3, s3, 0x24e00
	v_mov_b32_e32 v1, s3
	ds_read_u8 v2, v1
	v_lshrrev_b32_e32 v6, 3, v0
	v_bfe_u32 v4, v0, 2, 4
	v_and_or_b32 v1, v6, 48, v4
	v_mov_b32_e32 v8, 0
	s_waitcnt lgkmcnt(0)
	v_readfirstlane_b32 s6, v2
	s_lshl_b32 s3, s6, 2
	s_add_i32 s3, s3, 0
	s_add_i32 s7, s3, 0x24d00
	v_mov_b32_e32 v2, s7
	ds_read_b32 v2, v2
	s_add_i32 s3, s3, 0x25000
	v_mov_b32_e32 v3, s3
	ds_read_b32 v3, v3
	s_lshl_b32 s3, s33, 8
	s_ashr_i32 s7, s6, 31
	s_waitcnt lgkmcnt(1)
	v_readfirstlane_b32 s10, v2
	s_sub_i32 s12, s3, s10
	s_lshl_b64 s[6:7], s[6:7], 17
	s_waitcnt lgkmcnt(0)
	v_readfirstlane_b32 s3, v3
	s_add_u32 s6, s4, s6
	v_add_u32_e32 v2, s12, v1
	s_addc_u32 s7, s5, s7
	v_cmp_gt_i32_e32 vcc, s3, v2
	v_ashrrev_i32_e32 v3, 31, v2
	v_mov_b32_e32 v9, 0
	v_mov_b32_e32 v40, 0
	v_mov_b32_e32 v41, 0
	v_mov_b32_e32 v42, 0
	v_mov_b32_e32 v43, 0
	s_and_saveexec_b64 s[10:11], vcc
	s_cbranch_execz .LBB0_981
	v_lshl_add_u64 v[10:11], v[2:3], 2, s[6:7]
	global_load_dword v40, v[10:11], off
.LBB0_981:
	s_or_b64 exec, exec, s[10:11]
	v_bfe_u32 v5, v0, 3, 25
	v_or_b32_e32 v7, 64, v5
	s_movk_i32 s10, 0x70
	v_and_or_b32 v149, v7, s10, v4
	v_add_u32_e32 v4, s12, v149
	v_cmp_gt_i32_e32 vcc, s3, v4
	v_ashrrev_i32_e32 v5, 31, v4
	s_and_saveexec_b64 s[10:11], vcc
	s_cbranch_execz .LBB0_983
	v_lshl_add_u64 v[10:11], v[4:5], 2, s[6:7]
	global_load_dword v41, v[10:11], off
.LBB0_983:
	s_or_b64 exec, exec, s[10:11]
	s_addk_i32 s12, 0x80
	v_add_u32_e32 v10, s12, v1
	v_cmp_gt_i32_e32 vcc, s3, v10
	v_mov_b32_e32 v10, 0
	v_mov_b32_e32 v11, 0
	s_and_saveexec_b64 s[10:11], vcc
	s_cbranch_execz .LBB0_985
	v_lshl_add_u64 v[2:3], v[2:3], 2, s[6:7]
	global_load_dword v42, v[2:3], off offset:512
.LBB0_985:
	s_or_b64 exec, exec, s[10:11]
	v_add_u32_e32 v12, s12, v149
	v_lshrrev_b32_e32 v2, 2, v0
	v_lshlrev_b32_e32 v3, 4, v0
	v_cmp_gt_i32_e32 vcc, s3, v12
	s_and_saveexec_b64 s[10:11], vcc
	s_cbranch_execz .LBB0_987
	v_lshl_add_u64 v[4:5], v[4:5], 2, s[6:7]
	global_load_dword v43, v[4:5], off offset:512
.LBB0_987:
	s_or_b64 exec, exec, s[10:11]
	s_waitcnt vmcnt(0)
	v_lshlrev_b32_e32 v9, 12, v40
	v_lshlrev_b32_e32 v8, 12, v41
	v_lshlrev_b32_e32 v11, 12, v42
	v_lshlrev_b32_e32 v10, 12, v43
	s_ashr_i32 s37, s36, 31
	v_and_b32_e32 v4, 32, v0
	s_lshl_b64 s[10:11], s[36:37], 20
	v_bitop3_b32 v3, v3, v4, 48 bitop3:0x6c
	s_add_u32 s16, s22, 0x19000000
	v_and_or_b32 v151, v0, 64, v3
	s_addc_u32 s17, s23, 0
	v_lshlrev_b32_e32 v3, 1, v2
	v_lshrrev_b32_e32 v4, 5, v0
	s_add_u32 s42, s22, 0x4000000
	v_and_b32_e32 v3, 24, v3
	v_and_b32_e32 v4, 4, v4
	v_and_b32_e32 v2, 3, v2
	s_addc_u32 s43, s23, 0
	s_lshr_b32 s6, s2, 6
	v_or3_b32 v2, v4, v2, v3
	s_movk_i32 s3, 0x60
	v_and_or_b32 v3, v6, 32, v2
	v_and_or_b32 v2, v7, s3, v2
	s_lshr_b32 s3, s2, 8
	s_lshl_b32 s48, s6, 10
	s_add_u32 s38, s42, s10
	s_addc_u32 s39, s43, s11
	s_add_i32 s49, s48, 0
	v_lshl_or_b32 v132, v3, 12, v151
	s_add_i32 m0, s49, 0x10000
	v_lshl_or_b32 v134, v2, 12, v151
	global_load_lds_dwordx4 v132, s[38:39]
	s_add_i32 m0, s49, 0x12000
	s_add_u32 s10, s38, 0x80000
	global_load_lds_dwordx4 v134, s[38:39]
	s_addc_u32 s11, s39, 0
	s_add_i32 m0, s49, 0x14000
	v_or_b32_e32 v130, v9, v151
	global_load_lds_dwordx4 v132, s[10:11]
	s_add_i32 m0, s49, 0x16000
	s_add_i32 s50, s49, 0x2000
	global_load_lds_dwordx4 v134, s[10:11]
	s_mov_b32 m0, s49
	v_or_b32_e32 v140, v8, v151
	global_load_lds_dwordx4 v130, s[16:17]
	s_mov_b32 m0, s50
	s_add_i32 s51, s49, 0x4000
	v_or_b32_e32 v138, v11, v151
	global_load_lds_dwordx4 v140, s[16:17]
	s_mov_b32 m0, s51
	s_add_i32 s52, s49, 0x6000
	v_or_b32_e32 v142, v10, v151
	global_load_lds_dwordx4 v138, s[16:17]
	s_mov_b32 m0, s52
	v_mov_b32_e32 v131, 0
	global_load_lds_dwordx4 v142, s[16:17]
	v_mov_b32_e32 v133, v131
	v_mov_b32_e32 v135, v131
	s_cmp_eq_u32 s3, 1
	s_mov_b32 s53, 0
	v_lshl_add_u64 v[4:5], s[38:39], 0, v[132:133]
	v_lshl_add_u64 v[2:3], s[38:39], 0, v[134:135]
	s_cselect_b64 s[18:19], -1, 0
	s_cmp_lg_u32 s3, 1
	v_mov_b32_e32 v141, v131
	s_cbranch_scc1 .LBB0_989
	s_barrier
